# near-tie rescoring (fetch + fp64 pick of up to 3 queued entries per wave) moved before the END barrier, only exact-row stores after it; on top of Y0 deferral
# baseline (speedup 1.0000x reference)
.LBB1_65:
	s_lshl_b32 s88, s33, 5
	s_add_i32 s88, s88, s98
	s_add_i32 s88, s88, 0x18004
	s_lshl_b32 s88, s88, 10
	s_add_u32 s88, s14, s88
	s_addc_u32 s89, s15, 0
	s_add_u32 s90, s88, 0x2000
	s_addc_u32 s91, s89, 0
	s_add_u32 s92, s90, 0x2000
	s_addc_u32 s93, s91, 0
	s_add_u32 s94, s92, 0x2000
	s_addc_u32 s95, s93, 0
	v_readlane_b32 s52, v14, 0
	v_readlane_b32 s53, v14, 1
	v_readlane_b32 s54, v14, 2
	v_readlane_b32 s55, v14, 3
	v_readlane_b32 s56, v14, 4
	v_readlane_b32 s57, v14, 5
	v_readlane_b32 s58, v14, 6
	v_readlane_b32 s59, v14, 7
	v_readlane_b32 s68, v14, 8
	v_readlane_b32 s69, v14, 9
	v_readlane_b32 s70, v14, 10
	v_readlane_b32 s71, v14, 11
	v_readlane_b32 s72, v14, 12
	v_readlane_b32 s73, v14, 13
	v_readlane_b32 s74, v14, 14
	v_readlane_b32 s75, v14, 15
	v_readlane_b32 s76, v14, 16
	v_readlane_b32 s77, v14, 17
	v_readlane_b32 s78, v14, 18
	v_readlane_b32 s79, v14, 19
	v_readlane_b32 s80, v14, 20
	v_readlane_b32 s81, v14, 21
	v_readlane_b32 s82, v14, 22
	v_readlane_b32 s83, v14, 23
	v_readlane_b32 s84, v14, 24
	v_readlane_b32 s85, v14, 25
	v_readlane_b32 s86, v14, 26
	v_readlane_b32 s87, v14, 27
	v_readlane_b32 s96, v14, 28
	v_readlane_b32 s97, v14, 29
	v_readlane_b32 s99, v14, 30
	v_readlane_b32 s100, v14, 31
	s_mov_b64 exec, -1
	v_mbcnt_lo_u32_b32 v200, -1, 0
	v_mbcnt_hi_u32_b32 v200, -1, v200
	v_lshlrev_b32_e32 v201, 4, v200
	v_xor_b32_e32 v202, 32, v200
	v_lshlrev_b32_e32 v202, 2, v202
	v_xor_b32_e32 v203, 16, v200
	v_lshlrev_b32_e32 v203, 2, v203
	v_xor_b32_e32 v204, 8, v200
	v_lshlrev_b32_e32 v204, 2, v204
	v_xor_b32_e32 v205, 4, v200
	v_lshlrev_b32_e32 v205, 2, v205
	v_xor_b32_e32 v206, 2, v200
	v_lshlrev_b32_e32 v206, 2, v206
	v_xor_b32_e32 v207, 1, v200
	v_lshlrev_b32_e32 v207, 2, v207
	v_mov_b32_e32 v208, 0x22630
	ds_read_b32 v208, v208
	s_mov_b32 s51, s33
	s_waitcnt lgkmcnt(0)
	v_readfirstlane_b32 s50, v208
	s_nop 3
	s_mov_b32 s48, 0
	s_add_i32 s49, s51, 0
	s_cmp_lt_i32 s49, s50
	s_cbranch_scc0 .Lpt_fd_c
	s_lshl_b32 s60, s49, 2
	s_add_i32 s61, s60, 0x21800
	s_add_i32 s60, s60, 0x21000
	v_mov_b32_e32 v208, s61
	v_mov_b32_e32 v209, s60
	ds_read_b32 v208, v208
	ds_read_b32 v209, v209
	s_waitcnt lgkmcnt(0)
	v_readfirstlane_b32 s40, v208
	v_readfirstlane_b32 s44, v209
	s_nop 3
	s_lshl_b32 s62, s40, 10
	s_add_u32 s62, s16, s62
	s_addc_u32 s63, s17, 0
	global_load_dwordx4 v[2:5], v201, s[62:63]
	s_and_b32 s64, s44, 0x1ff
	s_bfe_u32 s65, s44, 0x90009
	s_bfe_u32 s66, s44, 0x90012
	v_lshl_or_b32 v210, s64, 10, v201
	v_lshl_or_b32 v211, s65, 10, v201
	v_lshl_or_b32 v212, s66, 10, v201
	global_load_dwordx4 v[6:9], v210, s[18:19]
	global_load_dwordx4 v[10:13], v211, s[18:19]
	global_load_dwordx4 v[14:17], v212, s[18:19]
	s_mov_b32 s48, 1
	s_add_i32 s49, s51, 8
	s_cmp_lt_i32 s49, s50
	s_cbranch_scc0 .Lpt_fd_c
	s_lshl_b32 s60, s49, 2
	s_add_i32 s61, s60, 0x21800
	s_add_i32 s60, s60, 0x21000
	v_mov_b32_e32 v208, s61
	v_mov_b32_e32 v209, s60
	ds_read_b32 v208, v208
	ds_read_b32 v209, v209
	s_waitcnt lgkmcnt(0)
	v_readfirstlane_b32 s41, v208
	v_readfirstlane_b32 s45, v209
	s_nop 3
	s_lshl_b32 s62, s41, 10
	s_add_u32 s62, s16, s62
	s_addc_u32 s63, s17, 0
	global_load_dwordx4 v[18:21], v201, s[62:63]
	s_and_b32 s64, s45, 0x1ff
	s_bfe_u32 s65, s45, 0x90009
	s_bfe_u32 s66, s45, 0x90012
	v_lshl_or_b32 v210, s64, 10, v201
	v_lshl_or_b32 v211, s65, 10, v201
	v_lshl_or_b32 v212, s66, 10, v201
	global_load_dwordx4 v[22:25], v210, s[18:19]
	global_load_dwordx4 v[26:29], v211, s[18:19]
	global_load_dwordx4 v[30:33], v212, s[18:19]
	s_mov_b32 s48, 2
	s_add_i32 s49, s51, 16
	s_cmp_lt_i32 s49, s50
	s_cbranch_scc0 .Lpt_fd_c
	s_lshl_b32 s60, s49, 2
	s_add_i32 s61, s60, 0x21800
	s_add_i32 s60, s60, 0x21000
	v_mov_b32_e32 v208, s61
	v_mov_b32_e32 v209, s60
	ds_read_b32 v208, v208
	ds_read_b32 v209, v209
	s_waitcnt lgkmcnt(0)
	v_readfirstlane_b32 s42, v208
	v_readfirstlane_b32 s46, v209
	s_nop 3
	s_lshl_b32 s62, s42, 10
	s_add_u32 s62, s16, s62
	s_addc_u32 s63, s17, 0
	global_load_dwordx4 v[34:37], v201, s[62:63]
	s_and_b32 s64, s46, 0x1ff
	s_bfe_u32 s65, s46, 0x90009
	s_bfe_u32 s66, s46, 0x90012
	v_lshl_or_b32 v210, s64, 10, v201
	v_lshl_or_b32 v211, s65, 10, v201
	v_lshl_or_b32 v212, s66, 10, v201
	global_load_dwordx4 v[38:41], v210, s[18:19]
	global_load_dwordx4 v[42:45], v211, s[18:19]
	global_load_dwordx4 v[46:49], v212, s[18:19]
	s_mov_b32 s48, 3
.Lpt_fd_c:
	v_lshl_or_b32 v192, s52, 10, v162
	v_lshl_or_b32 v193, s53, 10, v162
	v_lshl_or_b32 v194, s54, 10, v162
	v_lshl_or_b32 v195, s55, 10, v162
	v_lshl_or_b32 v196, s56, 10, v162
	v_lshl_or_b32 v197, s57, 10, v162
	v_lshl_or_b32 v198, s58, 10, v162
	v_lshl_or_b32 v199, s59, 10, v162
	global_load_dwordx4 v[50:53], v192, s[18:19]
	global_load_dwordx4 v[54:57], v193, s[18:19]
	global_load_dwordx4 v[58:61], v194, s[18:19]
	global_load_dwordx4 v[62:65], v195, s[18:19]
	global_load_dwordx4 v[66:69], v196, s[18:19]
	global_load_dwordx4 v[70:73], v197, s[18:19]
	global_load_dwordx4 v[74:77], v198, s[18:19]
	global_load_dwordx4 v[78:81], v199, s[18:19]
	v_lshl_or_b32 v192, s68, 10, v162
	v_lshl_or_b32 v193, s69, 10, v162
	v_lshl_or_b32 v194, s70, 10, v162
	v_lshl_or_b32 v195, s71, 10, v162
	v_lshl_or_b32 v196, s72, 10, v162
	v_lshl_or_b32 v197, s73, 10, v162
	v_lshl_or_b32 v198, s74, 10, v162
	v_lshl_or_b32 v199, s75, 10, v162
	global_load_dwordx4 v[82:85], v192, s[18:19]
	global_load_dwordx4 v[86:89], v193, s[18:19]
	global_load_dwordx4 v[90:93], v194, s[18:19]
	global_load_dwordx4 v[94:97], v195, s[18:19]
	global_load_dwordx4 v[98:101], v196, s[18:19]
	global_load_dwordx4 v[102:105], v197, s[18:19]
	global_load_dwordx4 v[106:109], v198, s[18:19]
	global_load_dwordx4 v[110:113], v199, s[18:19]
	v_lshl_or_b32 v192, s76, 10, v162
	v_lshl_or_b32 v193, s77, 10, v162
	v_lshl_or_b32 v194, s78, 10, v162
	v_lshl_or_b32 v195, s79, 10, v162
	v_lshl_or_b32 v196, s80, 10, v162
	v_lshl_or_b32 v197, s81, 10, v162
	v_lshl_or_b32 v198, s82, 10, v162
	v_lshl_or_b32 v199, s83, 10, v162
	global_load_dwordx4 v[114:117], v192, s[18:19]
	global_load_dwordx4 v[118:121], v193, s[18:19]
	global_load_dwordx4 v[122:125], v194, s[18:19]
	global_load_dwordx4 v[126:129], v195, s[18:19]
	global_load_dwordx4 v[130:133], v196, s[18:19]
	global_load_dwordx4 v[134:137], v197, s[18:19]
	global_load_dwordx4 v[138:141], v198, s[18:19]
	global_load_dwordx4 v[142:145], v199, s[18:19]
	v_lshl_or_b32 v192, s84, 10, v162
	v_lshl_or_b32 v193, s85, 10, v162
	v_lshl_or_b32 v194, s86, 10, v162
	v_lshl_or_b32 v195, s87, 10, v162
	v_lshl_or_b32 v196, s96, 10, v162
	v_lshl_or_b32 v197, s97, 10, v162
	v_lshl_or_b32 v198, s99, 10, v162
	v_lshl_or_b32 v199, s100, 10, v162
	global_load_dwordx4 v[146:149], v192, s[18:19]
	global_load_dwordx4 v[150:153], v193, s[18:19]
	global_load_dwordx4 v[154:157], v194, s[18:19]
	global_load_dwordx4 v[158:161], v195, s[18:19]
	global_load_dwordx4 v[176:179], v196, s[18:19]
	global_load_dwordx4 v[180:183], v197, s[18:19]
	global_load_dwordx4 v[184:187], v198, s[18:19]
	global_load_dwordx4 v[188:191], v199, s[18:19]
	s_waitcnt vmcnt(31)
	global_store_dwordx4 v162, v[50:53], s[88:89] offset:-4096 nt
	s_waitcnt vmcnt(31)
	global_store_dwordx4 v162, v[54:57], s[88:89] offset:-3072 nt
	s_waitcnt vmcnt(31)
	global_store_dwordx4 v162, v[58:61], s[88:89] offset:-2048 nt
	s_waitcnt vmcnt(31)
	global_store_dwordx4 v162, v[62:65], s[88:89] offset:-1024 nt
	s_waitcnt vmcnt(31)
	global_store_dwordx4 v162, v[66:69], s[88:89] offset:0 nt
	s_waitcnt vmcnt(31)
	global_store_dwordx4 v162, v[70:73], s[88:89] offset:1024 nt
	s_waitcnt vmcnt(31)
	global_store_dwordx4 v162, v[74:77], s[88:89] offset:2048 nt
	s_waitcnt vmcnt(31)
	global_store_dwordx4 v162, v[78:81], s[88:89] offset:3072 nt
	s_waitcnt vmcnt(31)
	global_store_dwordx4 v162, v[82:85], s[90:91] offset:-4096 nt
	s_waitcnt vmcnt(31)
	global_store_dwordx4 v162, v[86:89], s[90:91] offset:-3072 nt
	s_waitcnt vmcnt(31)
	global_store_dwordx4 v162, v[90:93], s[90:91] offset:-2048 nt
	s_waitcnt vmcnt(31)
	global_store_dwordx4 v162, v[94:97], s[90:91] offset:-1024 nt
	s_waitcnt vmcnt(31)
	global_store_dwordx4 v162, v[98:101], s[90:91] offset:0 nt
	s_waitcnt vmcnt(31)
	global_store_dwordx4 v162, v[102:105], s[90:91] offset:1024 nt
	s_waitcnt vmcnt(31)
	global_store_dwordx4 v162, v[106:109], s[90:91] offset:2048 nt
	s_waitcnt vmcnt(31)
	global_store_dwordx4 v162, v[110:113], s[90:91] offset:3072 nt
	s_waitcnt vmcnt(31)
	global_store_dwordx4 v162, v[114:117], s[92:93] offset:-4096 nt
	s_waitcnt vmcnt(31)
	global_store_dwordx4 v162, v[118:121], s[92:93] offset:-3072 nt
	s_waitcnt vmcnt(31)
	global_store_dwordx4 v162, v[122:125], s[92:93] offset:-2048 nt
	s_waitcnt vmcnt(31)
	global_store_dwordx4 v162, v[126:129], s[92:93] offset:-1024 nt
	s_waitcnt vmcnt(31)
	global_store_dwordx4 v162, v[130:133], s[92:93] offset:0 nt
	s_waitcnt vmcnt(31)
	global_store_dwordx4 v162, v[134:137], s[92:93] offset:1024 nt
	s_waitcnt vmcnt(31)
	global_store_dwordx4 v162, v[138:141], s[92:93] offset:2048 nt
	s_waitcnt vmcnt(31)
	global_store_dwordx4 v162, v[142:145], s[92:93] offset:3072 nt
	s_waitcnt vmcnt(31)
	global_store_dwordx4 v162, v[146:149], s[94:95] offset:-4096 nt
	s_waitcnt vmcnt(31)
	global_store_dwordx4 v162, v[150:153], s[94:95] offset:-3072 nt
	s_waitcnt vmcnt(31)
	global_store_dwordx4 v162, v[154:157], s[94:95] offset:-2048 nt
	s_waitcnt vmcnt(31)
	global_store_dwordx4 v162, v[158:161], s[94:95] offset:-1024 nt
	s_waitcnt vmcnt(31)
	global_store_dwordx4 v162, v[176:179], s[94:95] offset:0 nt
	s_waitcnt vmcnt(31)
	global_store_dwordx4 v162, v[180:183], s[94:95] offset:1024 nt
	s_waitcnt vmcnt(31)
	global_store_dwordx4 v162, v[184:187], s[94:95] offset:2048 nt
	s_waitcnt vmcnt(31)
	global_store_dwordx4 v162, v[188:191], s[94:95] offset:3072 nt
	s_waitcnt vmcnt(63)
	s_branch .Lpt_picks
	s_branch .LBB1_5

.LBB1_113:
	s_mov_b32 s9, 0
	s_branch .LBB1_116
	v_mov_b32_e32 v1, 0x22630
	ds_read_b32 v130, v1
	s_mov_b32 s9, 0
	s_waitcnt lgkmcnt(0)
	v_cmp_gt_i32_e32 vcc, 8, v130
	s_cbranch_vccnz .LBB1_115
	v_mov_b32_e32 v130, 0x2181c
	v_mov_b32_e32 v131, 0x2101c
	ds_read_b32 v130, v130
	ds_read_b32 v131, v131
	s_waitcnt lgkmcnt(1)
	v_readfirstlane_b32 s4, v130
	s_waitcnt lgkmcnt(0)
	v_readfirstlane_b32 s3, v131
	s_ashr_i32 s5, s4, 31
	s_and_b32 s13, s3, 0x1ff
	s_bfe_u32 s12, s3, 0x90009
	s_bfe_u32 s22, s3, 0x90012
	s_lshl_b64 s[6:7], s[4:5], 10
	s_add_u32 s4, s16, s6
	s_addc_u32 s5, s17, s7
	v_lshl_or_b32 v130, s13, 10, v162
	global_load_dwordx4 v[142:145], v162, s[4:5]
	v_lshl_or_b32 v131, s12, 10, v162
	global_load_dwordx4 v[134:137], v130, s[18:19]
	global_load_dwordx4 v[138:141], v131, s[18:19]
	v_lshl_or_b32 v130, s22, 10, v162
	global_load_dwordx4 v[130:133], v130, s[18:19]
	s_and_b32 s3, s3, 0x18000000
	s_cmp_eq_u32 s3, 0x10000000
	s_cselect_b64 s[4:5], -1, 0
	s_branch .LBB1_116

.LBB1_116:
	s_add_i32 s8, s98, 0x10060
	v_lshl_add_u64 v[146:147], s[14:15], 0, v[162:163]
	s_lshl_b64 s[10:11], s[8:9], 10
	s_add_i32 s8, s98, 0x10061
	v_lshl_add_u64 v[148:149], v[146:147], 0, s[10:11]
	s_lshl_b64 s[10:11], s[8:9], 10
	s_add_i32 s8, s98, 0x10062
	s_waitcnt vmcnt(47)
	global_store_dwordx4 v[148:149], v[26:29], off nt
	s_nop 1
	v_lshl_add_u64 v[26:27], v[146:147], 0, s[10:11]
	s_lshl_b64 s[10:11], s[8:9], 10
	s_add_i32 s8, s98, 0x10063
	s_waitcnt vmcnt(47)
	global_store_dwordx4 v[26:27], v[18:21], off nt
	s_nop 1
	v_lshl_add_u64 v[18:19], v[146:147], 0, s[10:11]
	s_lshl_b64 s[10:11], s[8:9], 10
	s_add_i32 s8, s98, 0x10064
	s_waitcnt vmcnt(47)
	global_store_dwordx4 v[18:19], v[10:13], off nt
	s_nop 1
	v_lshl_add_u64 v[10:11], v[146:147], 0, s[10:11]
	s_lshl_b64 s[10:11], s[8:9], 10
	s_add_i32 s8, s98, 0x10065
	s_waitcnt vmcnt(47)
	global_store_dwordx4 v[10:11], v[2:5], off nt
	s_nop 1
	v_lshl_add_u64 v[2:3], v[146:147], 0, s[10:11]
	s_lshl_b64 s[10:11], s[8:9], 10
	s_add_i32 s8, s98, 0x10066
	s_waitcnt vmcnt(38)
	global_store_dwordx4 v[2:3], v[30:33], off nt
	v_lshl_add_u64 v[2:3], v[146:147], 0, s[10:11]
	s_lshl_b64 s[10:11], s[8:9], 10
	s_add_i32 s8, s98, 0x10067
	global_store_dwordx4 v[2:3], v[14:17], off nt
	v_lshl_add_u64 v[2:3], v[146:147], 0, s[10:11]
	s_lshl_b64 s[10:11], s[8:9], 10
	s_add_i32 s8, s98, 0x10068
	global_store_dwordx4 v[2:3], v[6:9], off nt
	v_lshl_add_u64 v[2:3], v[146:147], 0, s[10:11]
	s_lshl_b64 s[10:11], s[8:9], 10
	s_add_i32 s8, s98, 0x10069
	global_store_dwordx4 v[2:3], v[22:25], off nt
	v_lshl_add_u64 v[2:3], v[146:147], 0, s[10:11]
	s_lshl_b64 s[10:11], s[8:9], 10
	s_add_i32 s8, s98, 0x1006a
	s_waitcnt vmcnt(41)
	global_store_dwordx4 v[2:3], v[58:61], off nt
	v_lshl_add_u64 v[2:3], v[146:147], 0, s[10:11]
	s_lshl_b64 s[10:11], s[8:9], 10
	s_add_i32 s8, s98, 0x1006b
	global_store_dwordx4 v[2:3], v[54:57], off nt
	v_lshl_add_u64 v[2:3], v[146:147], 0, s[10:11]
	s_lshl_b64 s[10:11], s[8:9], 10
	s_add_i32 s8, s98, 0x1006c
	global_store_dwordx4 v[2:3], v[46:49], off nt
	v_lshl_add_u64 v[2:3], v[146:147], 0, s[10:11]
	s_lshl_b64 s[10:11], s[8:9], 10
	s_add_i32 s8, s98, 0x1006d
	global_store_dwordx4 v[2:3], v[34:37], off nt
	v_lshl_add_u64 v[2:3], v[146:147], 0, s[10:11]
	s_lshl_b64 s[10:11], s[8:9], 10
	s_add_i32 s8, s98, 0x1006e
	s_waitcnt vmcnt(44)
	global_store_dwordx4 v[2:3], v[62:65], off nt
	v_lshl_add_u64 v[2:3], v[146:147], 0, s[10:11]
	s_lshl_b64 s[10:11], s[8:9], 10
	s_add_i32 s8, s98, 0x1006f
	global_store_dwordx4 v[2:3], v[50:53], off nt
	v_lshl_add_u64 v[2:3], v[146:147], 0, s[10:11]
	s_lshl_b64 s[10:11], s[8:9], 10
	s_add_i32 s8, s98, 0x10070
	global_store_dwordx4 v[2:3], v[42:45], off nt
	v_lshl_add_u64 v[2:3], v[146:147], 0, s[10:11]
	s_lshl_b64 s[10:11], s[8:9], 10
	s_add_i32 s8, s98, 0x10071
	global_store_dwordx4 v[2:3], v[38:41], off nt
	v_lshl_add_u64 v[2:3], v[146:147], 0, s[10:11]
	s_lshl_b64 s[10:11], s[8:9], 10
	s_add_i32 s8, s98, 0x10072
	s_waitcnt vmcnt(31)
	global_store_dwordx4 v[2:3], v[78:81], off nt
	v_lshl_add_u64 v[2:3], v[146:147], 0, s[10:11]
	s_lshl_b64 s[10:11], s[8:9], 10
	s_add_i32 s8, s98, 0x10073
	s_waitcnt vmcnt(31)
	global_store_dwordx4 v[2:3], v[74:77], off nt
	v_lshl_add_u64 v[2:3], v[146:147], 0, s[10:11]
	s_lshl_b64 s[10:11], s[8:9], 10
	s_add_i32 s8, s98, 0x10074
	s_waitcnt vmcnt(31)
	global_store_dwordx4 v[2:3], v[70:73], off nt
	v_lshl_add_u64 v[2:3], v[146:147], 0, s[10:11]
	s_lshl_b64 s[10:11], s[8:9], 10
	s_add_i32 s8, s98, 0x10075
	s_waitcnt vmcnt(31)
	global_store_dwordx4 v[2:3], v[66:69], off nt
	v_lshl_add_u64 v[2:3], v[146:147], 0, s[10:11]
	s_lshl_b64 s[10:11], s[8:9], 10
	s_add_i32 s8, s98, 0x10076
	s_waitcnt vmcnt(22)
	global_store_dwordx4 v[2:3], v[118:121], off nt
	v_lshl_add_u64 v[2:3], v[146:147], 0, s[10:11]
	s_lshl_b64 s[10:11], s[8:9], 10
	s_add_i32 s8, s98, 0x10077
	global_store_dwordx4 v[2:3], v[86:89], off nt
	v_lshl_add_u64 v[2:3], v[146:147], 0, s[10:11]
	s_lshl_b64 s[10:11], s[8:9], 10
	s_add_i32 s8, s98, 0x10078
	global_store_dwordx4 v[2:3], v[82:85], off nt
	v_lshl_add_u64 v[2:3], v[146:147], 0, s[10:11]
	s_lshl_b64 s[10:11], s[8:9], 10
	s_add_i32 s8, s98, 0x10079
	global_store_dwordx4 v[2:3], v[90:93], off nt
	v_lshl_add_u64 v[2:3], v[146:147], 0, s[10:11]
	s_lshl_b64 s[10:11], s[8:9], 10
	s_add_i32 s8, s98, 0x1007a
	s_waitcnt vmcnt(25)
	global_store_dwordx4 v[2:3], v[126:129], off nt
	v_lshl_add_u64 v[2:3], v[146:147], 0, s[10:11]
	s_lshl_b64 s[10:11], s[8:9], 10
	s_add_i32 s8, s98, 0x1007b
	global_store_dwordx4 v[2:3], v[102:105], off nt
	v_lshl_add_u64 v[2:3], v[146:147], 0, s[10:11]
	s_lshl_b64 s[10:11], s[8:9], 10
	s_add_i32 s8, s98, 0x1007c
	global_store_dwordx4 v[2:3], v[98:101], off nt
	v_lshl_add_u64 v[2:3], v[146:147], 0, s[10:11]
	s_lshl_b64 s[10:11], s[8:9], 10
	s_add_i32 s8, s98, 0x1007d
	global_store_dwordx4 v[2:3], v[94:97], off nt
	v_lshl_add_u64 v[2:3], v[146:147], 0, s[10:11]
	s_lshl_b64 s[10:11], s[8:9], 10
	s_add_i32 s8, s98, 0x1007e
	s_waitcnt vmcnt(28)
	global_store_dwordx4 v[2:3], v[122:125], off nt
	v_lshl_add_u64 v[2:3], v[146:147], 0, s[10:11]
	s_lshl_b64 s[10:11], s[8:9], 10
	s_add_i32 s8, s98, 0x1007f
	global_store_dwordx4 v[2:3], v[110:113], off nt
	v_lshl_add_u64 v[2:3], v[146:147], 0, s[10:11]
	s_lshl_b64 s[8:9], s[8:9], 10
	global_store_dwordx4 v[2:3], v[106:109], off nt
	v_lshl_add_u64 v[2:3], v[146:147], 0, s[8:9]
	global_store_dwordx4 v[2:3], v[114:117], off nt
	s_branch .Lhelper_tail
	s_waitcnt vmcnt(0) expcnt(0) lgkmcnt(0)
	s_barrier
	ds_read_b32 v1, v1
	s_waitcnt lgkmcnt(0)
	v_cmp_lt_i32_e32 vcc, 7, v1
	v_readfirstlane_b32 s3, v1
	s_cbranch_vccz .LBB1_128
	v_cvt_f64_f32_e32 v[4:5], v134
	v_cvt_f64_f32_e32 v[2:3], v142
	v_fma_f64 v[6:7], -2.0, v[2:3], v[4:5]
	v_mul_f64 v[10:11], v[6:7], v[4:5]
	v_cvt_f64_f32_e32 v[6:7], v135
	v_cvt_f64_f32_e32 v[4:5], v143
	v_mbcnt_lo_u32_b32 v1, -1, 0
	v_fma_f64 v[8:9], -2.0, v[4:5], v[6:7]
	v_mbcnt_hi_u32_b32 v22, -1, v1
	v_fmac_f64_e32 v[10:11], v[6:7], v[8:9]
	v_cvt_f64_f32_e32 v[8:9], v136
	v_cvt_f64_f32_e32 v[6:7], v144
	v_and_b32_e32 v1, 64, v22
	v_fma_f64 v[12:13], -2.0, v[6:7], v[8:9]
	v_add_u32_e32 v23, 64, v1
	v_xor_b32_e32 v1, 32, v22
	v_fmac_f64_e32 v[10:11], v[8:9], v[12:13]
	v_cvt_f64_f32_e32 v[12:13], v137
	v_cvt_f64_f32_e32 v[8:9], v145
	v_cmp_lt_i32_e32 vcc, v1, v23
	v_fma_f64 v[14:15], -2.0, v[8:9], v[12:13]
	v_fmac_f64_e32 v[10:11], v[12:13], v[14:15]
	v_cndmask_b32_e32 v1, v22, v1, vcc
	v_lshlrev_b32_e32 v1, 2, v1
	ds_bpermute_b32 v12, v1, v10
	ds_bpermute_b32 v13, v1, v11
	v_xor_b32_e32 v20, 4, v22
	v_xor_b32_e32 v24, 1, v22
	s_waitcnt lgkmcnt(0)
	v_add_f64 v[10:11], v[10:11], v[12:13]
	v_xor_b32_e32 v12, 16, v22
	v_cmp_lt_i32_e32 vcc, v12, v23
	s_nop 1
	v_cndmask_b32_e32 v12, v22, v12, vcc
	v_lshlrev_b32_e32 v14, 2, v12
	ds_bpermute_b32 v12, v14, v10
	ds_bpermute_b32 v13, v14, v11
	s_waitcnt lgkmcnt(0)
	v_add_f64 v[10:11], v[10:11], v[12:13]
	v_xor_b32_e32 v12, 8, v22
	v_cmp_lt_i32_e32 vcc, v12, v23
	s_nop 1
	v_cndmask_b32_e32 v12, v22, v12, vcc
	v_lshlrev_b32_e32 v15, 2, v12
	ds_bpermute_b32 v12, v15, v10
	ds_bpermute_b32 v13, v15, v11
	v_cmp_lt_i32_e32 vcc, v20, v23
	s_waitcnt lgkmcnt(0)
	v_add_f64 v[10:11], v[10:11], v[12:13]
	v_cvt_f64_f32_e32 v[12:13], v138
	v_fma_f64 v[16:17], -2.0, v[2:3], v[12:13]
	v_mul_f64 v[12:13], v[16:17], v[12:13]
	v_cvt_f64_f32_e32 v[16:17], v139
	v_fma_f64 v[18:19], -2.0, v[4:5], v[16:17]
	v_fmac_f64_e32 v[12:13], v[16:17], v[18:19]
	v_cvt_f64_f32_e32 v[16:17], v140
	v_fma_f64 v[18:19], -2.0, v[6:7], v[16:17]
	v_fmac_f64_e32 v[12:13], v[16:17], v[18:19]
	v_cvt_f64_f32_e32 v[16:17], v141
	v_fma_f64 v[18:19], -2.0, v[8:9], v[16:17]
	v_fmac_f64_e32 v[12:13], v[16:17], v[18:19]
	ds_bpermute_b32 v18, v1, v12
	ds_bpermute_b32 v19, v1, v13
	v_cndmask_b32_e32 v16, v22, v20, vcc
	v_lshlrev_b32_e32 v16, 2, v16
	ds_bpermute_b32 v20, v16, v10
	ds_bpermute_b32 v21, v16, v11
	s_waitcnt lgkmcnt(2)
	v_add_f64 v[12:13], v[12:13], v[18:19]
	ds_bpermute_b32 v18, v14, v12
	ds_bpermute_b32 v19, v14, v13
	v_xor_b32_e32 v17, 2, v22
	v_cmp_lt_i32_e32 vcc, v17, v23
	s_waitcnt lgkmcnt(2)
	v_add_f64 v[10:11], v[10:11], v[20:21]
	s_waitcnt lgkmcnt(0)
	v_add_f64 v[12:13], v[12:13], v[18:19]
	ds_bpermute_b32 v18, v15, v12
	ds_bpermute_b32 v19, v15, v13
	v_cndmask_b32_e32 v17, v22, v17, vcc
	v_lshlrev_b32_e32 v17, 2, v17
	ds_bpermute_b32 v20, v17, v10
	ds_bpermute_b32 v21, v17, v11
	s_waitcnt lgkmcnt(2)
	v_add_f64 v[12:13], v[12:13], v[18:19]
	ds_bpermute_b32 v18, v16, v12
	ds_bpermute_b32 v19, v16, v13
	v_cmp_lt_i32_e32 vcc, v24, v23
	s_waitcnt lgkmcnt(2)
	v_add_f64 v[10:11], v[10:11], v[20:21]
	s_waitcnt lgkmcnt(0)
	v_add_f64 v[12:13], v[12:13], v[18:19]
	ds_bpermute_b32 v20, v17, v12
	ds_bpermute_b32 v21, v17, v13
	v_cndmask_b32_e32 v18, v22, v24, vcc
	v_lshlrev_b32_e32 v19, 2, v18
	ds_bpermute_b32 v22, v19, v10
	ds_bpermute_b32 v23, v19, v11
	s_waitcnt lgkmcnt(2)
	v_add_f64 v[12:13], v[12:13], v[20:21]
	ds_bpermute_b32 v20, v19, v12
	ds_bpermute_b32 v21, v19, v13
	s_waitcnt lgkmcnt(2)
	v_add_f64 v[10:11], v[10:11], v[22:23]
	s_waitcnt lgkmcnt(0)
	v_add_f64 v[12:13], v[12:13], v[20:21]
	v_cmp_lt_f64_e64 s[8:9], v[12:13], v[10:11]
	v_cmp_nlt_f64_e32 vcc, v[12:13], v[10:11]
	s_and_saveexec_b64 s[10:11], vcc
	s_cbranch_execnz .LBB1_120
	s_or_b64 exec, exec, s[10:11]
	v_mov_b32_e32 v18, s13
	s_and_saveexec_b64 s[10:11], s[8:9]
	s_cbranch_execnz .LBB1_121

.LBB1_154:
	s_branch .Lhelper_tail
	v_mov_b32_e32 v1, 0x22630
	ds_read_b32 v2, v1
	s_waitcnt lgkmcnt(0)
	v_cmp_ge_i32_e32 vcc, s33, v2
	s_cbranch_vccnz .LBB1_156
	s_lshl_b32 s2, s33, 2
	s_add_i32 s3, s2, 0x21800
	s_add_i32 s2, s2, 0x21000
	v_mov_b32_e32 v2, s3
	v_mov_b32_e32 v3, s2
	ds_read_b32 v2, v2
	ds_read_b32 v3, v3
	s_waitcnt lgkmcnt(1)
	v_readfirstlane_b32 s2, v2
	s_waitcnt lgkmcnt(0)
	v_readfirstlane_b32 s6, v3
	s_ashr_i32 s3, s2, 31
	s_and_b32 s12, s6, 0x1ff
	s_bfe_u32 s11, s6, 0x90009
	s_bfe_u32 s13, s6, 0x90012
	s_lshl_b64 s[4:5], s[2:3], 10
	s_add_u32 s2, s16, s4
	s_addc_u32 s3, s17, s5
	v_lshl_or_b32 v10, s12, 10, v162
	global_load_dwordx4 v[14:17], v162, s[2:3]
	v_lshl_or_b32 v11, s11, 10, v162
	global_load_dwordx4 v[2:5], v10, s[18:19]
	global_load_dwordx4 v[6:9], v11, s[18:19]
	v_lshl_or_b32 v10, s13, 10, v162
	global_load_dwordx4 v[10:13], v10, s[18:19]
	s_and_b32 s2, s6, 0x18000000
	s_cmp_eq_u32 s2, 0x10000000
	s_cselect_b64 s[2:3], -1, 0
	s_branch .LBB1_157

.LBB1_195:
	s_branch .Lhelper_tail
	v_mov_b32_e32 v16, 0x22630
	ds_read_b32 v0, v16
	s_waitcnt lgkmcnt(0)
	v_cmp_gt_i32_e32 vcc, 5, v0
	s_cbranch_vccnz .LBB1_197
	v_mov_b32_e32 v0, 0x21810
	v_mov_b32_e32 v1, 0x21010
	ds_read_b32 v0, v0
	ds_read_b32 v1, v1
	s_waitcnt lgkmcnt(1)
	v_readfirstlane_b32 s0, v0
	s_waitcnt lgkmcnt(0)
	v_readfirstlane_b32 s4, v1
	s_ashr_i32 s1, s0, 31
	s_and_b32 s10, s4, 0x1ff
	s_bfe_u32 s9, s4, 0x90009
	s_bfe_u32 s11, s4, 0x90012
	s_lshl_b64 s[2:3], s[0:1], 10
	s_add_u32 s0, s16, s2
	s_addc_u32 s1, s17, s3
	v_lshl_or_b32 v8, s10, 10, v162
	global_load_dwordx4 v[12:15], v162, s[0:1]
	v_lshl_or_b32 v9, s9, 10, v162
	global_load_dwordx4 v[0:3], v8, s[18:19]
	global_load_dwordx4 v[4:7], v9, s[18:19]
	v_lshl_or_b32 v8, s11, 10, v162
	global_load_dwordx4 v[8:11], v8, s[18:19]
	s_and_b32 s0, s4, 0x18000000
	s_cmp_eq_u32 s0, 0x10000000
	s_cselect_b64 s[0:1], -1, 0
	s_branch .LBB1_198

.Lhelper_tail:
	s_mov_b64 exec, -1
	v_mbcnt_lo_u32_b32 v200, -1, 0
	v_mbcnt_hi_u32_b32 v200, -1, v200
	v_lshlrev_b32_e32 v201, 4, v200
	v_xor_b32_e32 v202, 32, v200
	v_lshlrev_b32_e32 v202, 2, v202
	v_xor_b32_e32 v203, 16, v200
	v_lshlrev_b32_e32 v203, 2, v203
	v_xor_b32_e32 v204, 8, v200
	v_lshlrev_b32_e32 v204, 2, v204
	v_xor_b32_e32 v205, 4, v200
	v_lshlrev_b32_e32 v205, 2, v205
	v_xor_b32_e32 v206, 2, v200
	v_lshlrev_b32_e32 v206, 2, v206
	v_xor_b32_e32 v207, 1, v200
	v_lshlrev_b32_e32 v207, 2, v207
	v_mov_b32_e32 v208, 0x22630
	ds_read_b32 v208, v208
	s_mov_b32 s51, s33
	s_waitcnt lgkmcnt(0)
	v_readfirstlane_b32 s50, v208
	s_nop 3
	s_mov_b32 s48, 0
	s_add_i32 s49, s51, 0
	s_cmp_lt_i32 s49, s50
	s_cbranch_scc0 .Lpt_fd_h
	s_lshl_b32 s60, s49, 2
	s_add_i32 s61, s60, 0x21800
	s_add_i32 s60, s60, 0x21000
	v_mov_b32_e32 v208, s61
	v_mov_b32_e32 v209, s60
	ds_read_b32 v208, v208
	ds_read_b32 v209, v209
	s_waitcnt lgkmcnt(0)
	v_readfirstlane_b32 s40, v208
	v_readfirstlane_b32 s44, v209
	s_nop 3
	s_lshl_b32 s62, s40, 10
	s_add_u32 s62, s16, s62
	s_addc_u32 s63, s17, 0
	global_load_dwordx4 v[2:5], v201, s[62:63]
	s_and_b32 s64, s44, 0x1ff
	s_bfe_u32 s65, s44, 0x90009
	s_bfe_u32 s66, s44, 0x90012
	v_lshl_or_b32 v210, s64, 10, v201
	v_lshl_or_b32 v211, s65, 10, v201
	v_lshl_or_b32 v212, s66, 10, v201
	global_load_dwordx4 v[6:9], v210, s[18:19]
	global_load_dwordx4 v[10:13], v211, s[18:19]
	global_load_dwordx4 v[14:17], v212, s[18:19]
	s_mov_b32 s48, 1
	s_add_i32 s49, s51, 8
	s_cmp_lt_i32 s49, s50
	s_cbranch_scc0 .Lpt_fd_h
	s_lshl_b32 s60, s49, 2
	s_add_i32 s61, s60, 0x21800
	s_add_i32 s60, s60, 0x21000
	v_mov_b32_e32 v208, s61
	v_mov_b32_e32 v209, s60
	ds_read_b32 v208, v208
	ds_read_b32 v209, v209
	s_waitcnt lgkmcnt(0)
	v_readfirstlane_b32 s41, v208
	v_readfirstlane_b32 s45, v209
	s_nop 3
	s_lshl_b32 s62, s41, 10
	s_add_u32 s62, s16, s62
	s_addc_u32 s63, s17, 0
	global_load_dwordx4 v[18:21], v201, s[62:63]
	s_and_b32 s64, s45, 0x1ff
	s_bfe_u32 s65, s45, 0x90009
	s_bfe_u32 s66, s45, 0x90012
	v_lshl_or_b32 v210, s64, 10, v201
	v_lshl_or_b32 v211, s65, 10, v201
	v_lshl_or_b32 v212, s66, 10, v201
	global_load_dwordx4 v[22:25], v210, s[18:19]
	global_load_dwordx4 v[26:29], v211, s[18:19]
	global_load_dwordx4 v[30:33], v212, s[18:19]
	s_mov_b32 s48, 2
	s_add_i32 s49, s51, 16
	s_cmp_lt_i32 s49, s50
	s_cbranch_scc0 .Lpt_fd_h
	s_lshl_b32 s60, s49, 2
	s_add_i32 s61, s60, 0x21800
	s_add_i32 s60, s60, 0x21000
	v_mov_b32_e32 v208, s61
	v_mov_b32_e32 v209, s60
	ds_read_b32 v208, v208
	ds_read_b32 v209, v209
	s_waitcnt lgkmcnt(0)
	v_readfirstlane_b32 s42, v208
	v_readfirstlane_b32 s46, v209
	s_nop 3
	s_lshl_b32 s62, s42, 10
	s_add_u32 s62, s16, s62
	s_addc_u32 s63, s17, 0
	global_load_dwordx4 v[34:37], v201, s[62:63]
	s_and_b32 s64, s46, 0x1ff
	s_bfe_u32 s65, s46, 0x90009
	s_bfe_u32 s66, s46, 0x90012
	v_lshl_or_b32 v210, s64, 10, v201
	v_lshl_or_b32 v211, s65, 10, v201
	v_lshl_or_b32 v212, s66, 10, v201
	global_load_dwordx4 v[38:41], v210, s[18:19]
	global_load_dwordx4 v[42:45], v211, s[18:19]
	global_load_dwordx4 v[46:49], v212, s[18:19]
	s_mov_b32 s48, 3

.Lpt_picks:
	s_cmp_lt_u32 0, s48
	s_cbranch_scc0 .Lpt_pd
	v_cvt_f64_f32_e32 v[66:67], v2
	v_cvt_f64_f32_e32 v[68:69], v3
	v_cvt_f64_f32_e32 v[70:71], v4
	v_cvt_f64_f32_e32 v[72:73], v5
	v_cvt_f64_f32_e32 v[80:81], v6
	v_fma_f64 v[82:83], -2.0, v[66:67], v[80:81]
	v_mul_f64 v[74:75], v[82:83], v[80:81]
	v_cvt_f64_f32_e32 v[80:81], v7
	v_fma_f64 v[82:83], -2.0, v[68:69], v[80:81]
	v_fmac_f64_e32 v[74:75], v[80:81], v[82:83]
	v_cvt_f64_f32_e32 v[80:81], v8
	v_fma_f64 v[82:83], -2.0, v[70:71], v[80:81]
	v_fmac_f64_e32 v[74:75], v[80:81], v[82:83]
	v_cvt_f64_f32_e32 v[80:81], v9
	v_fma_f64 v[82:83], -2.0, v[72:73], v[80:81]
	v_fmac_f64_e32 v[74:75], v[80:81], v[82:83]
	v_cvt_f64_f32_e32 v[80:81], v10
	v_fma_f64 v[82:83], -2.0, v[66:67], v[80:81]
	v_mul_f64 v[76:77], v[82:83], v[80:81]
	v_cvt_f64_f32_e32 v[80:81], v11
	v_fma_f64 v[82:83], -2.0, v[68:69], v[80:81]
	v_fmac_f64_e32 v[76:77], v[80:81], v[82:83]
	v_cvt_f64_f32_e32 v[80:81], v12
	v_fma_f64 v[82:83], -2.0, v[70:71], v[80:81]
	v_fmac_f64_e32 v[76:77], v[80:81], v[82:83]
	v_cvt_f64_f32_e32 v[80:81], v13
	v_fma_f64 v[82:83], -2.0, v[72:73], v[80:81]
	v_fmac_f64_e32 v[76:77], v[80:81], v[82:83]
	v_cvt_f64_f32_e32 v[80:81], v14
	v_fma_f64 v[82:83], -2.0, v[66:67], v[80:81]
	v_mul_f64 v[78:79], v[82:83], v[80:81]
	v_cvt_f64_f32_e32 v[80:81], v15
	v_fma_f64 v[82:83], -2.0, v[68:69], v[80:81]
	v_fmac_f64_e32 v[78:79], v[80:81], v[82:83]
	v_cvt_f64_f32_e32 v[80:81], v16
	v_fma_f64 v[82:83], -2.0, v[70:71], v[80:81]
	v_fmac_f64_e32 v[78:79], v[80:81], v[82:83]
	v_cvt_f64_f32_e32 v[80:81], v17
	v_fma_f64 v[82:83], -2.0, v[72:73], v[80:81]
	v_fmac_f64_e32 v[78:79], v[80:81], v[82:83]
	ds_bpermute_b32 v84, v202, v74
	ds_bpermute_b32 v85, v202, v75
	ds_bpermute_b32 v86, v202, v76
	ds_bpermute_b32 v87, v202, v77
	ds_bpermute_b32 v88, v202, v78
	ds_bpermute_b32 v89, v202, v79
	s_waitcnt lgkmcnt(0)
	v_add_f64 v[74:75], v[74:75], v[84:85]
	v_add_f64 v[76:77], v[76:77], v[86:87]
	v_add_f64 v[78:79], v[78:79], v[88:89]
	ds_bpermute_b32 v84, v203, v74
	ds_bpermute_b32 v85, v203, v75
	ds_bpermute_b32 v86, v203, v76
	ds_bpermute_b32 v87, v203, v77
	ds_bpermute_b32 v88, v203, v78
	ds_bpermute_b32 v89, v203, v79
	s_waitcnt lgkmcnt(0)
	v_add_f64 v[74:75], v[74:75], v[84:85]
	v_add_f64 v[76:77], v[76:77], v[86:87]
	v_add_f64 v[78:79], v[78:79], v[88:89]
	ds_bpermute_b32 v84, v204, v74
	ds_bpermute_b32 v85, v204, v75
	ds_bpermute_b32 v86, v204, v76
	ds_bpermute_b32 v87, v204, v77
	ds_bpermute_b32 v88, v204, v78
	ds_bpermute_b32 v89, v204, v79
	s_waitcnt lgkmcnt(0)
	v_add_f64 v[74:75], v[74:75], v[84:85]
	v_add_f64 v[76:77], v[76:77], v[86:87]
	v_add_f64 v[78:79], v[78:79], v[88:89]
	ds_bpermute_b32 v84, v205, v74
	ds_bpermute_b32 v85, v205, v75
	ds_bpermute_b32 v86, v205, v76
	ds_bpermute_b32 v87, v205, v77
	ds_bpermute_b32 v88, v205, v78
	ds_bpermute_b32 v89, v205, v79
	s_waitcnt lgkmcnt(0)
	v_add_f64 v[74:75], v[74:75], v[84:85]
	v_add_f64 v[76:77], v[76:77], v[86:87]
	v_add_f64 v[78:79], v[78:79], v[88:89]
	ds_bpermute_b32 v84, v206, v74
	ds_bpermute_b32 v85, v206, v75
	ds_bpermute_b32 v86, v206, v76
	ds_bpermute_b32 v87, v206, v77
	ds_bpermute_b32 v88, v206, v78
	ds_bpermute_b32 v89, v206, v79
	s_waitcnt lgkmcnt(0)
	v_add_f64 v[74:75], v[74:75], v[84:85]
	v_add_f64 v[76:77], v[76:77], v[86:87]
	v_add_f64 v[78:79], v[78:79], v[88:89]
	ds_bpermute_b32 v84, v207, v74
	ds_bpermute_b32 v85, v207, v75
	ds_bpermute_b32 v86, v207, v76
	ds_bpermute_b32 v87, v207, v77
	ds_bpermute_b32 v88, v207, v78
	ds_bpermute_b32 v89, v207, v79
	s_waitcnt lgkmcnt(0)
	v_add_f64 v[74:75], v[74:75], v[84:85]
	v_add_f64 v[76:77], v[76:77], v[86:87]
	v_add_f64 v[78:79], v[78:79], v[88:89]
	s_and_b32 s60, s44, 0x1ff
	s_bfe_u32 s61, s44, 0x90009
	s_bfe_u32 s62, s44, 0x90012
	s_bfe_u32 s63, s44, 0x2001b
	s_mov_b32 s64, s60
	v_cmp_lt_f64_e64 s[70:71], v[76:77], v[74:75]
	v_cmp_eq_f64_e64 s[72:73], v[76:77], v[74:75]
	s_cmp_lt_i32 s61, s64
	s_cselect_b64 s[74:75], -1, 0
	s_and_b64 s[72:73], s[72:73], s[74:75]
	s_or_b64 s[70:71], s[70:71], s[72:73]
	s_cmp_lg_u64 s[70:71], 0
	s_cbranch_scc0 .Lpt_kb_g_0
	v_mov_b32_e32 v74, v76
	v_mov_b32_e32 v75, v77
	s_mov_b32 s64, s61
.Lpt_kb_g_0:
	s_cmp_eq_u32 s63, 2
	s_cbranch_scc0 .Lpt_kc_g_0
	v_cmp_lt_f64_e64 s[70:71], v[78:79], v[74:75]
	v_cmp_eq_f64_e64 s[72:73], v[78:79], v[74:75]
	s_cmp_lt_i32 s62, s64
	s_cselect_b64 s[74:75], -1, 0
	s_and_b64 s[72:73], s[72:73], s[74:75]
	s_or_b64 s[70:71], s[70:71], s[72:73]
	s_cmp_lg_u64 s[70:71], 0
	s_cbranch_scc0 .Lpt_kc_g_0
	s_mov_b32 s64, s62
.Lpt_kc_g_0:
	s_mov_b32 s76, s64
	s_cmp_lt_u32 1, s48
	s_cbranch_scc0 .Lpt_pd
	v_cvt_f64_f32_e32 v[66:67], v18
	v_cvt_f64_f32_e32 v[68:69], v19
	v_cvt_f64_f32_e32 v[70:71], v20
	v_cvt_f64_f32_e32 v[72:73], v21
	v_cvt_f64_f32_e32 v[80:81], v22
	v_fma_f64 v[82:83], -2.0, v[66:67], v[80:81]
	v_mul_f64 v[74:75], v[82:83], v[80:81]
	v_cvt_f64_f32_e32 v[80:81], v23
	v_fma_f64 v[82:83], -2.0, v[68:69], v[80:81]
	v_fmac_f64_e32 v[74:75], v[80:81], v[82:83]
	v_cvt_f64_f32_e32 v[80:81], v24
	v_fma_f64 v[82:83], -2.0, v[70:71], v[80:81]
	v_fmac_f64_e32 v[74:75], v[80:81], v[82:83]
	v_cvt_f64_f32_e32 v[80:81], v25
	v_fma_f64 v[82:83], -2.0, v[72:73], v[80:81]
	v_fmac_f64_e32 v[74:75], v[80:81], v[82:83]
	v_cvt_f64_f32_e32 v[80:81], v26
	v_fma_f64 v[82:83], -2.0, v[66:67], v[80:81]
	v_mul_f64 v[76:77], v[82:83], v[80:81]
	v_cvt_f64_f32_e32 v[80:81], v27
	v_fma_f64 v[82:83], -2.0, v[68:69], v[80:81]
	v_fmac_f64_e32 v[76:77], v[80:81], v[82:83]
	v_cvt_f64_f32_e32 v[80:81], v28
	v_fma_f64 v[82:83], -2.0, v[70:71], v[80:81]
	v_fmac_f64_e32 v[76:77], v[80:81], v[82:83]
	v_cvt_f64_f32_e32 v[80:81], v29
	v_fma_f64 v[82:83], -2.0, v[72:73], v[80:81]
	v_fmac_f64_e32 v[76:77], v[80:81], v[82:83]
	v_cvt_f64_f32_e32 v[80:81], v30
	v_fma_f64 v[82:83], -2.0, v[66:67], v[80:81]
	v_mul_f64 v[78:79], v[82:83], v[80:81]
	v_cvt_f64_f32_e32 v[80:81], v31
	v_fma_f64 v[82:83], -2.0, v[68:69], v[80:81]
	v_fmac_f64_e32 v[78:79], v[80:81], v[82:83]
	v_cvt_f64_f32_e32 v[80:81], v32
	v_fma_f64 v[82:83], -2.0, v[70:71], v[80:81]
	v_fmac_f64_e32 v[78:79], v[80:81], v[82:83]
	v_cvt_f64_f32_e32 v[80:81], v33
	v_fma_f64 v[82:83], -2.0, v[72:73], v[80:81]
	v_fmac_f64_e32 v[78:79], v[80:81], v[82:83]
	ds_bpermute_b32 v84, v202, v74
	ds_bpermute_b32 v85, v202, v75
	ds_bpermute_b32 v86, v202, v76
	ds_bpermute_b32 v87, v202, v77
	ds_bpermute_b32 v88, v202, v78
	ds_bpermute_b32 v89, v202, v79
	s_waitcnt lgkmcnt(0)
	v_add_f64 v[74:75], v[74:75], v[84:85]
	v_add_f64 v[76:77], v[76:77], v[86:87]
	v_add_f64 v[78:79], v[78:79], v[88:89]
	ds_bpermute_b32 v84, v203, v74
	ds_bpermute_b32 v85, v203, v75
	ds_bpermute_b32 v86, v203, v76
	ds_bpermute_b32 v87, v203, v77
	ds_bpermute_b32 v88, v203, v78
	ds_bpermute_b32 v89, v203, v79
	s_waitcnt lgkmcnt(0)
	v_add_f64 v[74:75], v[74:75], v[84:85]
	v_add_f64 v[76:77], v[76:77], v[86:87]
	v_add_f64 v[78:79], v[78:79], v[88:89]
	ds_bpermute_b32 v84, v204, v74
	ds_bpermute_b32 v85, v204, v75
	ds_bpermute_b32 v86, v204, v76
	ds_bpermute_b32 v87, v204, v77
	ds_bpermute_b32 v88, v204, v78
	ds_bpermute_b32 v89, v204, v79
	s_waitcnt lgkmcnt(0)
	v_add_f64 v[74:75], v[74:75], v[84:85]
	v_add_f64 v[76:77], v[76:77], v[86:87]
	v_add_f64 v[78:79], v[78:79], v[88:89]
	ds_bpermute_b32 v84, v205, v74
	ds_bpermute_b32 v85, v205, v75
	ds_bpermute_b32 v86, v205, v76
	ds_bpermute_b32 v87, v205, v77
	ds_bpermute_b32 v88, v205, v78
	ds_bpermute_b32 v89, v205, v79
	s_waitcnt lgkmcnt(0)
	v_add_f64 v[74:75], v[74:75], v[84:85]
	v_add_f64 v[76:77], v[76:77], v[86:87]
	v_add_f64 v[78:79], v[78:79], v[88:89]
	ds_bpermute_b32 v84, v206, v74
	ds_bpermute_b32 v85, v206, v75
	ds_bpermute_b32 v86, v206, v76
	ds_bpermute_b32 v87, v206, v77
	ds_bpermute_b32 v88, v206, v78
	ds_bpermute_b32 v89, v206, v79
	s_waitcnt lgkmcnt(0)
	v_add_f64 v[74:75], v[74:75], v[84:85]
	v_add_f64 v[76:77], v[76:77], v[86:87]
	v_add_f64 v[78:79], v[78:79], v[88:89]
	ds_bpermute_b32 v84, v207, v74
	ds_bpermute_b32 v85, v207, v75
	ds_bpermute_b32 v86, v207, v76
	ds_bpermute_b32 v87, v207, v77
	ds_bpermute_b32 v88, v207, v78
	ds_bpermute_b32 v89, v207, v79
	s_waitcnt lgkmcnt(0)
	v_add_f64 v[74:75], v[74:75], v[84:85]
	v_add_f64 v[76:77], v[76:77], v[86:87]
	v_add_f64 v[78:79], v[78:79], v[88:89]
	s_and_b32 s60, s45, 0x1ff
	s_bfe_u32 s61, s45, 0x90009
	s_bfe_u32 s62, s45, 0x90012
	s_bfe_u32 s63, s45, 0x2001b
	s_mov_b32 s64, s60
	v_cmp_lt_f64_e64 s[70:71], v[76:77], v[74:75]
	v_cmp_eq_f64_e64 s[72:73], v[76:77], v[74:75]
	s_cmp_lt_i32 s61, s64
	s_cselect_b64 s[74:75], -1, 0
	s_and_b64 s[72:73], s[72:73], s[74:75]
	s_or_b64 s[70:71], s[70:71], s[72:73]
	s_cmp_lg_u64 s[70:71], 0
	s_cbranch_scc0 .Lpt_kb_g_1
	v_mov_b32_e32 v74, v76
	v_mov_b32_e32 v75, v77
	s_mov_b32 s64, s61

.Lpt_kc_g_1:
	s_mov_b32 s77, s64
	s_cmp_lt_u32 2, s48
	s_cbranch_scc0 .Lpt_pd
	v_cvt_f64_f32_e32 v[66:67], v34
	v_cvt_f64_f32_e32 v[68:69], v35
	v_cvt_f64_f32_e32 v[70:71], v36
	v_cvt_f64_f32_e32 v[72:73], v37
	v_cvt_f64_f32_e32 v[80:81], v38
	v_fma_f64 v[82:83], -2.0, v[66:67], v[80:81]
	v_mul_f64 v[74:75], v[82:83], v[80:81]
	v_cvt_f64_f32_e32 v[80:81], v39
	v_fma_f64 v[82:83], -2.0, v[68:69], v[80:81]
	v_fmac_f64_e32 v[74:75], v[80:81], v[82:83]
	v_cvt_f64_f32_e32 v[80:81], v40
	v_fma_f64 v[82:83], -2.0, v[70:71], v[80:81]
	v_fmac_f64_e32 v[74:75], v[80:81], v[82:83]
	v_cvt_f64_f32_e32 v[80:81], v41
	v_fma_f64 v[82:83], -2.0, v[72:73], v[80:81]
	v_fmac_f64_e32 v[74:75], v[80:81], v[82:83]
	v_cvt_f64_f32_e32 v[80:81], v42
	v_fma_f64 v[82:83], -2.0, v[66:67], v[80:81]
	v_mul_f64 v[76:77], v[82:83], v[80:81]
	v_cvt_f64_f32_e32 v[80:81], v43
	v_fma_f64 v[82:83], -2.0, v[68:69], v[80:81]
	v_fmac_f64_e32 v[76:77], v[80:81], v[82:83]
	v_cvt_f64_f32_e32 v[80:81], v44
	v_fma_f64 v[82:83], -2.0, v[70:71], v[80:81]
	v_fmac_f64_e32 v[76:77], v[80:81], v[82:83]
	v_cvt_f64_f32_e32 v[80:81], v45
	v_fma_f64 v[82:83], -2.0, v[72:73], v[80:81]
	v_fmac_f64_e32 v[76:77], v[80:81], v[82:83]
	v_cvt_f64_f32_e32 v[80:81], v46
	v_fma_f64 v[82:83], -2.0, v[66:67], v[80:81]
	v_mul_f64 v[78:79], v[82:83], v[80:81]
	v_cvt_f64_f32_e32 v[80:81], v47
	v_fma_f64 v[82:83], -2.0, v[68:69], v[80:81]
	v_fmac_f64_e32 v[78:79], v[80:81], v[82:83]
	v_cvt_f64_f32_e32 v[80:81], v48
	v_fma_f64 v[82:83], -2.0, v[70:71], v[80:81]
	v_fmac_f64_e32 v[78:79], v[80:81], v[82:83]
	v_cvt_f64_f32_e32 v[80:81], v49
	v_fma_f64 v[82:83], -2.0, v[72:73], v[80:81]
	v_fmac_f64_e32 v[78:79], v[80:81], v[82:83]
	ds_bpermute_b32 v84, v202, v74
	ds_bpermute_b32 v85, v202, v75
	ds_bpermute_b32 v86, v202, v76
	ds_bpermute_b32 v87, v202, v77
	ds_bpermute_b32 v88, v202, v78
	ds_bpermute_b32 v89, v202, v79
	s_waitcnt lgkmcnt(0)
	v_add_f64 v[74:75], v[74:75], v[84:85]
	v_add_f64 v[76:77], v[76:77], v[86:87]
	v_add_f64 v[78:79], v[78:79], v[88:89]
	ds_bpermute_b32 v84, v203, v74
	ds_bpermute_b32 v85, v203, v75
	ds_bpermute_b32 v86, v203, v76
	ds_bpermute_b32 v87, v203, v77
	ds_bpermute_b32 v88, v203, v78
	ds_bpermute_b32 v89, v203, v79
	s_waitcnt lgkmcnt(0)
	v_add_f64 v[74:75], v[74:75], v[84:85]
	v_add_f64 v[76:77], v[76:77], v[86:87]
	v_add_f64 v[78:79], v[78:79], v[88:89]
	ds_bpermute_b32 v84, v204, v74
	ds_bpermute_b32 v85, v204, v75
	ds_bpermute_b32 v86, v204, v76
	ds_bpermute_b32 v87, v204, v77
	ds_bpermute_b32 v88, v204, v78
	ds_bpermute_b32 v89, v204, v79
	s_waitcnt lgkmcnt(0)
	v_add_f64 v[74:75], v[74:75], v[84:85]
	v_add_f64 v[76:77], v[76:77], v[86:87]
	v_add_f64 v[78:79], v[78:79], v[88:89]
	ds_bpermute_b32 v84, v205, v74
	ds_bpermute_b32 v85, v205, v75
	ds_bpermute_b32 v86, v205, v76
	ds_bpermute_b32 v87, v205, v77
	ds_bpermute_b32 v88, v205, v78
	ds_bpermute_b32 v89, v205, v79
	s_waitcnt lgkmcnt(0)
	v_add_f64 v[74:75], v[74:75], v[84:85]
	v_add_f64 v[76:77], v[76:77], v[86:87]
	v_add_f64 v[78:79], v[78:79], v[88:89]
	ds_bpermute_b32 v84, v206, v74
	ds_bpermute_b32 v85, v206, v75
	ds_bpermute_b32 v86, v206, v76
	ds_bpermute_b32 v87, v206, v77
	ds_bpermute_b32 v88, v206, v78
	ds_bpermute_b32 v89, v206, v79
	s_waitcnt lgkmcnt(0)
	v_add_f64 v[74:75], v[74:75], v[84:85]
	v_add_f64 v[76:77], v[76:77], v[86:87]
	v_add_f64 v[78:79], v[78:79], v[88:89]
	ds_bpermute_b32 v84, v207, v74
	ds_bpermute_b32 v85, v207, v75
	ds_bpermute_b32 v86, v207, v76
	ds_bpermute_b32 v87, v207, v77
	ds_bpermute_b32 v88, v207, v78
	ds_bpermute_b32 v89, v207, v79
	s_waitcnt lgkmcnt(0)
	v_add_f64 v[74:75], v[74:75], v[84:85]
	v_add_f64 v[76:77], v[76:77], v[86:87]
	v_add_f64 v[78:79], v[78:79], v[88:89]
	s_and_b32 s60, s46, 0x1ff
	s_bfe_u32 s61, s46, 0x90009
	s_bfe_u32 s62, s46, 0x90012
	s_bfe_u32 s63, s46, 0x2001b
	s_mov_b32 s64, s60
	v_cmp_lt_f64_e64 s[70:71], v[76:77], v[74:75]
	v_cmp_eq_f64_e64 s[72:73], v[76:77], v[74:75]
	s_cmp_lt_i32 s61, s64
	s_cselect_b64 s[74:75], -1, 0
	s_and_b64 s[72:73], s[72:73], s[74:75]
	s_or_b64 s[70:71], s[70:71], s[72:73]
	s_cmp_lg_u64 s[70:71], 0
	s_cbranch_scc0 .Lpt_kb_g_2
	v_mov_b32_e32 v74, v76
	v_mov_b32_e32 v75, v77
	s_mov_b32 s64, s61

.Lpt_kc_g_2:
	s_mov_b32 s78, s64
.Lpt_pd:
	s_waitcnt vmcnt(0)
	s_barrier
	s_cmp_lt_u32 0, s48
	s_cbranch_scc0 .Lpt_sdone
	s_and_b32 s60, s44, 0x1ff
	s_bfe_u32 s61, s44, 0x90009
	s_lshl_b32 s66, s40, 10
	s_add_u32 s66, s14, s66
	s_addc_u32 s67, s15, 0
	s_cmp_eq_u32 s76, s60
	s_cbranch_scc0 .Lpt_nb_g_0
	global_store_dwordx4 v201, v[6:9], s[66:67]
	s_branch .Lpt_sd_g_0
.Lpt_nb_g_0:
	s_cmp_eq_u32 s76, s61
	s_cbranch_scc0 .Lpt_nc_g_0
	global_store_dwordx4 v201, v[10:13], s[66:67]
	s_branch .Lpt_sd_g_0
.Lpt_nc_g_0:
	global_store_dwordx4 v201, v[14:17], s[66:67]
.Lpt_sd_g_0:
	s_cmp_lt_u32 1, s48
	s_cbranch_scc0 .Lpt_sdone
	s_and_b32 s60, s45, 0x1ff
	s_bfe_u32 s61, s45, 0x90009
	s_lshl_b32 s66, s41, 10
	s_add_u32 s66, s14, s66
	s_addc_u32 s67, s15, 0
	s_cmp_eq_u32 s77, s60
	s_cbranch_scc0 .Lpt_nb_g_1
	global_store_dwordx4 v201, v[22:25], s[66:67]
	s_branch .Lpt_sd_g_1
.Lpt_nb_g_1:
	s_cmp_eq_u32 s77, s61
	s_cbranch_scc0 .Lpt_nc_g_1
	global_store_dwordx4 v201, v[26:29], s[66:67]
	s_branch .Lpt_sd_g_1
.Lpt_nc_g_1:
	global_store_dwordx4 v201, v[30:33], s[66:67]
.Lpt_sd_g_1:
	s_cmp_lt_u32 2, s48
	s_cbranch_scc0 .Lpt_sdone
	s_and_b32 s60, s46, 0x1ff
	s_bfe_u32 s61, s46, 0x90009
	s_lshl_b32 s66, s42, 10
	s_add_u32 s66, s14, s66
	s_addc_u32 s67, s15, 0
	s_cmp_eq_u32 s78, s60
	s_cbranch_scc0 .Lpt_nb_g_2
	global_store_dwordx4 v201, v[38:41], s[66:67]
	s_branch .Lpt_sd_g_2
.Lpt_nb_g_2:
	s_cmp_eq_u32 s78, s61
	s_cbranch_scc0 .Lpt_nc_g_2
	global_store_dwordx4 v201, v[42:45], s[66:67]
	s_branch .Lpt_sd_g_2
.Lpt_nc_g_2:
	global_store_dwordx4 v201, v[46:49], s[66:67]
.Lpt_sd_g_2:
.Lpt_sdone:
	s_add_i32 s52, s51, 24
.Lpt_loop:
	s_cmp_lt_i32 s52, s50
	s_cbranch_scc0 .LBB1_223
	s_mov_b32 s49, s52
	s_lshl_b32 s60, s49, 2
	s_add_i32 s61, s60, 0x21800
	s_add_i32 s60, s60, 0x21000
	v_mov_b32_e32 v208, s61
	v_mov_b32_e32 v209, s60
	ds_read_b32 v208, v208
	ds_read_b32 v209, v209
	s_waitcnt lgkmcnt(0)
	v_readfirstlane_b32 s40, v208
	v_readfirstlane_b32 s44, v209
	s_nop 3
	s_lshl_b32 s62, s40, 10
	s_add_u32 s62, s16, s62
	s_addc_u32 s63, s17, 0
	global_load_dwordx4 v[2:5], v201, s[62:63]
	s_and_b32 s64, s44, 0x1ff
	s_bfe_u32 s65, s44, 0x90009
	s_bfe_u32 s66, s44, 0x90012
	v_lshl_or_b32 v210, s64, 10, v201
	v_lshl_or_b32 v211, s65, 10, v201
	v_lshl_or_b32 v212, s66, 10, v201
	global_load_dwordx4 v[6:9], v210, s[18:19]
	global_load_dwordx4 v[10:13], v211, s[18:19]
	global_load_dwordx4 v[14:17], v212, s[18:19]
	s_waitcnt vmcnt(0)
	v_cvt_f64_f32_e32 v[66:67], v2
	v_cvt_f64_f32_e32 v[68:69], v3
	v_cvt_f64_f32_e32 v[70:71], v4
	v_cvt_f64_f32_e32 v[72:73], v5
	v_cvt_f64_f32_e32 v[80:81], v6
	v_fma_f64 v[82:83], -2.0, v[66:67], v[80:81]
	v_mul_f64 v[74:75], v[82:83], v[80:81]
	v_cvt_f64_f32_e32 v[80:81], v7
	v_fma_f64 v[82:83], -2.0, v[68:69], v[80:81]
	v_fmac_f64_e32 v[74:75], v[80:81], v[82:83]
	v_cvt_f64_f32_e32 v[80:81], v8
	v_fma_f64 v[82:83], -2.0, v[70:71], v[80:81]
	v_fmac_f64_e32 v[74:75], v[80:81], v[82:83]
	v_cvt_f64_f32_e32 v[80:81], v9
	v_fma_f64 v[82:83], -2.0, v[72:73], v[80:81]
	v_fmac_f64_e32 v[74:75], v[80:81], v[82:83]
	v_cvt_f64_f32_e32 v[80:81], v10
	v_fma_f64 v[82:83], -2.0, v[66:67], v[80:81]
	v_mul_f64 v[76:77], v[82:83], v[80:81]
	v_cvt_f64_f32_e32 v[80:81], v11
	v_fma_f64 v[82:83], -2.0, v[68:69], v[80:81]
	v_fmac_f64_e32 v[76:77], v[80:81], v[82:83]
	v_cvt_f64_f32_e32 v[80:81], v12
	v_fma_f64 v[82:83], -2.0, v[70:71], v[80:81]
	v_fmac_f64_e32 v[76:77], v[80:81], v[82:83]
	v_cvt_f64_f32_e32 v[80:81], v13
	v_fma_f64 v[82:83], -2.0, v[72:73], v[80:81]
	v_fmac_f64_e32 v[76:77], v[80:81], v[82:83]
	v_cvt_f64_f32_e32 v[80:81], v14
	v_fma_f64 v[82:83], -2.0, v[66:67], v[80:81]
	v_mul_f64 v[78:79], v[82:83], v[80:81]
	v_cvt_f64_f32_e32 v[80:81], v15
	v_fma_f64 v[82:83], -2.0, v[68:69], v[80:81]
	v_fmac_f64_e32 v[78:79], v[80:81], v[82:83]
	v_cvt_f64_f32_e32 v[80:81], v16
	v_fma_f64 v[82:83], -2.0, v[70:71], v[80:81]
	v_fmac_f64_e32 v[78:79], v[80:81], v[82:83]
	v_cvt_f64_f32_e32 v[80:81], v17
	v_fma_f64 v[82:83], -2.0, v[72:73], v[80:81]
	v_fmac_f64_e32 v[78:79], v[80:81], v[82:83]
	ds_bpermute_b32 v84, v202, v74
	ds_bpermute_b32 v85, v202, v75
	ds_bpermute_b32 v86, v202, v76
	ds_bpermute_b32 v87, v202, v77
	ds_bpermute_b32 v88, v202, v78
	ds_bpermute_b32 v89, v202, v79
	s_waitcnt lgkmcnt(0)
	v_add_f64 v[74:75], v[74:75], v[84:85]
	v_add_f64 v[76:77], v[76:77], v[86:87]
	v_add_f64 v[78:79], v[78:79], v[88:89]
	ds_bpermute_b32 v84, v203, v74
	ds_bpermute_b32 v85, v203, v75
	ds_bpermute_b32 v86, v203, v76
	ds_bpermute_b32 v87, v203, v77
	ds_bpermute_b32 v88, v203, v78
	ds_bpermute_b32 v89, v203, v79
	s_waitcnt lgkmcnt(0)
	v_add_f64 v[74:75], v[74:75], v[84:85]
	v_add_f64 v[76:77], v[76:77], v[86:87]
	v_add_f64 v[78:79], v[78:79], v[88:89]
	ds_bpermute_b32 v84, v204, v74
	ds_bpermute_b32 v85, v204, v75
	ds_bpermute_b32 v86, v204, v76
	ds_bpermute_b32 v87, v204, v77
	ds_bpermute_b32 v88, v204, v78
	ds_bpermute_b32 v89, v204, v79
	s_waitcnt lgkmcnt(0)
	v_add_f64 v[74:75], v[74:75], v[84:85]
	v_add_f64 v[76:77], v[76:77], v[86:87]
	v_add_f64 v[78:79], v[78:79], v[88:89]
	ds_bpermute_b32 v84, v205, v74
	ds_bpermute_b32 v85, v205, v75
	ds_bpermute_b32 v86, v205, v76
	ds_bpermute_b32 v87, v205, v77
	ds_bpermute_b32 v88, v205, v78
	ds_bpermute_b32 v89, v205, v79
	s_waitcnt lgkmcnt(0)
	v_add_f64 v[74:75], v[74:75], v[84:85]
	v_add_f64 v[76:77], v[76:77], v[86:87]
	v_add_f64 v[78:79], v[78:79], v[88:89]
	ds_bpermute_b32 v84, v206, v74
	ds_bpermute_b32 v85, v206, v75
	ds_bpermute_b32 v86, v206, v76
	ds_bpermute_b32 v87, v206, v77
	ds_bpermute_b32 v88, v206, v78
	ds_bpermute_b32 v89, v206, v79
	s_waitcnt lgkmcnt(0)
	v_add_f64 v[74:75], v[74:75], v[84:85]
	v_add_f64 v[76:77], v[76:77], v[86:87]
	v_add_f64 v[78:79], v[78:79], v[88:89]
	ds_bpermute_b32 v84, v207, v74
	ds_bpermute_b32 v85, v207, v75
	ds_bpermute_b32 v86, v207, v76
	ds_bpermute_b32 v87, v207, v77
	ds_bpermute_b32 v88, v207, v78
	ds_bpermute_b32 v89, v207, v79
	s_waitcnt lgkmcnt(0)
	v_add_f64 v[74:75], v[74:75], v[84:85]
	v_add_f64 v[76:77], v[76:77], v[86:87]
	v_add_f64 v[78:79], v[78:79], v[88:89]
	s_and_b32 s60, s44, 0x1ff
	s_bfe_u32 s61, s44, 0x90009
	s_bfe_u32 s62, s44, 0x90012
	s_bfe_u32 s63, s44, 0x2001b
	s_mov_b32 s64, s60
	v_cmp_lt_f64_e64 s[70:71], v[76:77], v[74:75]
	v_cmp_eq_f64_e64 s[72:73], v[76:77], v[74:75]
	s_cmp_lt_i32 s61, s64
	s_cselect_b64 s[74:75], -1, 0
	s_and_b64 s[72:73], s[72:73], s[74:75]
	s_or_b64 s[70:71], s[70:71], s[72:73]
	s_cmp_lg_u64 s[70:71], 0
	s_cbranch_scc0 .Lpt_kb_f_0
	v_mov_b32_e32 v74, v76
	v_mov_b32_e32 v75, v77
	s_mov_b32 s64, s61

.Lpt_kc_f_0:
	s_mov_b32 s76, s64
	s_and_b32 s60, s44, 0x1ff
	s_bfe_u32 s61, s44, 0x90009
	s_lshl_b32 s66, s40, 10
	s_add_u32 s66, s14, s66
	s_addc_u32 s67, s15, 0
	s_cmp_eq_u32 s76, s60
	s_cbranch_scc0 .Lpt_nb_f_0
	global_store_dwordx4 v201, v[6:9], s[66:67]
	s_branch .Lpt_sd_f_0

.Lpt_sd_f_0:
	s_add_i32 s52, s52, 8
	s_branch .Lpt_loop
